# adds MLA epilogue: shfl_down 1/2/3 as DPP quad permutes instead of ds_bpermute round trips
# speedup vs baseline: 1.0133x; 1.0018x over previous
.LBB0_725:
	s_lshl_b32 s0, s75, 7
	v_and_b32_e32 v1, 63, v222
	s_add_u32 s2, s97, s0
	s_nop 15
	s_nop 3
	v_cmp_ne_u32_e32 vcc, 63, v1
	s_addc_u32 s3, s78, 0
	s_nop 15
	s_nop 3
	s_ashr_i32 s75, s74, 31
	v_addc_co_u32_e32 v2, vcc, 0, v222, vcc
	s_nop 15
	s_nop 3
	s_lshl_b64 s[0:1], s[74:75], 10
	v_cmp_gt_u32_e32 vcc, 62, v1
	v_rcp_f32_e32 v9, v84
	s_add_u32 s0, s2, s0
	v_lshlrev_b32_e32 v6, 2, v2
	v_cndmask_b32_e64 v2, 0, 2, vcc
	s_addc_u32 s1, s3, s1
	v_add_lshl_u32 v7, v2, v222, 2
	v_cmp_gt_u32_e32 vcc, 61, v1
	v_lshlrev_b32_e32 v2, 12, v181
	v_mov_b32_e32 v181, v3
	v_cndmask_b32_e64 v1, 0, 3, vcc
	v_lshl_add_u64 v[4:5], s[0:1], 0, v[180:181]
	v_add_lshl_u32 v8, v1, v222, 2
	v_lshl_add_u64 v[4:5], v[4:5], 0, v[2:3]
	v_mul_f32_e32 v2, v68, v9
	s_nop 1
	v_mov_b32_dpp v11, v2 quad_perm:[1,1,1,1] row_mask:0xf bank_mask:0xf
	v_mov_b32_dpp v10, v2 quad_perm:[2,2,2,2] row_mask:0xf bank_mask:0xf
	v_mov_b32_dpp v12, v2 quad_perm:[3,3,3,3] row_mask:0xf bank_mask:0xf
	v_and_b32_e32 v1, 3, v19
	v_cmp_eq_u32_e64 s[6:7], 0, v1
	s_and_saveexec_b64 s[0:1], s[6:7]
	s_cbranch_execz .LBB0_727
	v_mov_b32_e32 v1, v3
	s_waitcnt lgkmcnt(0)
	v_cvt_pk_fp8_f32 v1, v2, v11
	v_cvt_pk_fp8_f32 v1, v10, v12 op_sel:[0,0,1]
	global_store_dword v[4:5], v1, off
.LBB0_727:
	s_or_b64 exec, exec, s[0:1]
	v_mul_f32_e32 v2, v52, v9
	s_waitcnt lgkmcnt(0)
	s_nop 1
	v_mov_b32_dpp v11, v2 quad_perm:[1,1,1,1] row_mask:0xf bank_mask:0xf
	v_mov_b32_dpp v10, v2 quad_perm:[2,2,2,2] row_mask:0xf bank_mask:0xf
	v_mov_b32_dpp v12, v2 quad_perm:[3,3,3,3] row_mask:0xf bank_mask:0xf
	s_and_saveexec_b64 s[0:1], s[6:7]
	s_cbranch_execz .LBB0_729
	v_mov_b32_e32 v1, v3
	s_waitcnt lgkmcnt(0)
	v_cvt_pk_fp8_f32 v1, v2, v11
	v_cvt_pk_fp8_f32 v1, v10, v12 op_sel:[0,0,1]
	global_store_dword v[4:5], v1, off offset:32
.LBB0_729:
	s_or_b64 exec, exec, s[0:1]
	v_mul_f32_e32 v2, v36, v9
	s_waitcnt lgkmcnt(0)
	s_nop 1
	v_mov_b32_dpp v11, v2 quad_perm:[1,1,1,1] row_mask:0xf bank_mask:0xf
	v_mov_b32_dpp v10, v2 quad_perm:[2,2,2,2] row_mask:0xf bank_mask:0xf
	v_mov_b32_dpp v12, v2 quad_perm:[3,3,3,3] row_mask:0xf bank_mask:0xf
	s_and_saveexec_b64 s[0:1], s[6:7]
	s_cbranch_execz .LBB0_731
	v_mov_b32_e32 v1, v3
	s_waitcnt lgkmcnt(0)
	v_cvt_pk_fp8_f32 v1, v2, v11
	v_cvt_pk_fp8_f32 v1, v10, v12 op_sel:[0,0,1]
	global_store_dword v[4:5], v1, off offset:64
.LBB0_731:
	s_or_b64 exec, exec, s[0:1]
	v_mul_f32_e32 v2, v20, v9
	s_waitcnt lgkmcnt(0)
	s_nop 1
	v_mov_b32_dpp v10, v2 quad_perm:[1,1,1,1] row_mask:0xf bank_mask:0xf
	v_mov_b32_dpp v9, v2 quad_perm:[2,2,2,2] row_mask:0xf bank_mask:0xf
	v_mov_b32_dpp v11, v2 quad_perm:[3,3,3,3] row_mask:0xf bank_mask:0xf
	s_and_saveexec_b64 s[0:1], s[6:7]
	s_cbranch_execz .LBB0_733
	v_mov_b32_e32 v1, v3
	s_waitcnt lgkmcnt(0)
	v_cvt_pk_fp8_f32 v1, v2, v10
	v_cvt_pk_fp8_f32 v1, v9, v11 op_sel:[0,0,1]
	global_store_dword v[4:5], v1, off offset:96
.LBB0_733:
	s_or_b64 exec, exec, s[0:1]
	v_rcp_f32_e32 v2, v85
	s_waitcnt lgkmcnt(0)
	v_mul_f32_e32 v9, v69, v2
	s_nop 1
	v_mov_b32_dpp v11, v9 quad_perm:[1,1,1,1] row_mask:0xf bank_mask:0xf
	v_mov_b32_dpp v10, v9 quad_perm:[2,2,2,2] row_mask:0xf bank_mask:0xf
	v_mov_b32_dpp v12, v9 quad_perm:[3,3,3,3] row_mask:0xf bank_mask:0xf
	s_and_saveexec_b64 s[0:1], s[6:7]
	s_cbranch_execz .LBB0_735
	v_mov_b32_e32 v1, v3
	s_waitcnt lgkmcnt(0)
	v_cvt_pk_fp8_f32 v1, v9, v11
	v_cvt_pk_fp8_f32 v1, v10, v12 op_sel:[0,0,1]
	global_store_dword v[4:5], v1, off offset:1024
.LBB0_735:
	s_or_b64 exec, exec, s[0:1]
	v_mul_f32_e32 v9, v53, v2
	s_waitcnt lgkmcnt(0)
	s_nop 1
	v_mov_b32_dpp v11, v9 quad_perm:[1,1,1,1] row_mask:0xf bank_mask:0xf
	v_mov_b32_dpp v10, v9 quad_perm:[2,2,2,2] row_mask:0xf bank_mask:0xf
	v_mov_b32_dpp v12, v9 quad_perm:[3,3,3,3] row_mask:0xf bank_mask:0xf
	s_and_saveexec_b64 s[0:1], s[6:7]
	s_cbranch_execz .LBB0_737
	v_mov_b32_e32 v1, v3
	s_waitcnt lgkmcnt(0)
	v_cvt_pk_fp8_f32 v1, v9, v11
	v_cvt_pk_fp8_f32 v1, v10, v12 op_sel:[0,0,1]
	global_store_dword v[4:5], v1, off offset:1056
.LBB0_737:
	s_or_b64 exec, exec, s[0:1]
	v_mul_f32_e32 v9, v37, v2
	s_waitcnt lgkmcnt(0)
	s_nop 1
	v_mov_b32_dpp v11, v9 quad_perm:[1,1,1,1] row_mask:0xf bank_mask:0xf
	v_mov_b32_dpp v10, v9 quad_perm:[2,2,2,2] row_mask:0xf bank_mask:0xf
	v_mov_b32_dpp v12, v9 quad_perm:[3,3,3,3] row_mask:0xf bank_mask:0xf
	s_and_saveexec_b64 s[0:1], s[6:7]
	s_cbranch_execz .LBB0_739
	v_mov_b32_e32 v1, v3
	s_waitcnt lgkmcnt(0)
	v_cvt_pk_fp8_f32 v1, v9, v11
	v_cvt_pk_fp8_f32 v1, v10, v12 op_sel:[0,0,1]
	global_store_dword v[4:5], v1, off offset:1088
.LBB0_739:
	s_or_b64 exec, exec, s[0:1]
	v_mul_f32_e32 v2, v21, v2
	s_waitcnt lgkmcnt(0)
	s_nop 1
	v_mov_b32_dpp v10, v2 quad_perm:[1,1,1,1] row_mask:0xf bank_mask:0xf
	v_mov_b32_dpp v9, v2 quad_perm:[2,2,2,2] row_mask:0xf bank_mask:0xf
	v_mov_b32_dpp v11, v2 quad_perm:[3,3,3,3] row_mask:0xf bank_mask:0xf
	s_and_saveexec_b64 s[0:1], s[6:7]
	s_cbranch_execz .LBB0_741
	v_mov_b32_e32 v1, v3
	s_waitcnt lgkmcnt(0)
	v_cvt_pk_fp8_f32 v1, v2, v10
	v_cvt_pk_fp8_f32 v1, v9, v11 op_sel:[0,0,1]
	global_store_dword v[4:5], v1, off offset:1120
.LBB0_741:
	s_or_b64 exec, exec, s[0:1]
	v_rcp_f32_e32 v2, v86
	s_waitcnt lgkmcnt(0)
	v_mul_f32_e32 v9, v70, v2
	s_nop 1
	v_mov_b32_dpp v11, v9 quad_perm:[1,1,1,1] row_mask:0xf bank_mask:0xf
	v_mov_b32_dpp v10, v9 quad_perm:[2,2,2,2] row_mask:0xf bank_mask:0xf
	v_mov_b32_dpp v12, v9 quad_perm:[3,3,3,3] row_mask:0xf bank_mask:0xf
	s_and_saveexec_b64 s[0:1], s[6:7]
	s_cbranch_execz .LBB0_743
	v_mov_b32_e32 v1, v3
	s_waitcnt lgkmcnt(0)
	v_cvt_pk_fp8_f32 v1, v9, v11
	v_cvt_pk_fp8_f32 v1, v10, v12 op_sel:[0,0,1]
	global_store_dword v[4:5], v1, off offset:2048
.LBB0_743:
	s_or_b64 exec, exec, s[0:1]
	v_mul_f32_e32 v9, v54, v2
	s_waitcnt lgkmcnt(0)
	s_nop 1
	v_mov_b32_dpp v11, v9 quad_perm:[1,1,1,1] row_mask:0xf bank_mask:0xf
	v_mov_b32_dpp v10, v9 quad_perm:[2,2,2,2] row_mask:0xf bank_mask:0xf
	v_mov_b32_dpp v12, v9 quad_perm:[3,3,3,3] row_mask:0xf bank_mask:0xf
	s_and_saveexec_b64 s[0:1], s[6:7]
	s_cbranch_execz .LBB0_745
	v_mov_b32_e32 v1, v3
	s_waitcnt lgkmcnt(0)
	v_cvt_pk_fp8_f32 v1, v9, v11
	v_cvt_pk_fp8_f32 v1, v10, v12 op_sel:[0,0,1]
	global_store_dword v[4:5], v1, off offset:2080
.LBB0_745:
	s_or_b64 exec, exec, s[0:1]
	v_mul_f32_e32 v9, v38, v2
	s_waitcnt lgkmcnt(0)
	s_nop 1
	v_mov_b32_dpp v11, v9 quad_perm:[1,1,1,1] row_mask:0xf bank_mask:0xf
	v_mov_b32_dpp v10, v9 quad_perm:[2,2,2,2] row_mask:0xf bank_mask:0xf
	v_mov_b32_dpp v12, v9 quad_perm:[3,3,3,3] row_mask:0xf bank_mask:0xf
	s_and_saveexec_b64 s[0:1], s[6:7]
	s_cbranch_execz .LBB0_747
	v_mov_b32_e32 v1, v3
	s_waitcnt lgkmcnt(0)
	v_cvt_pk_fp8_f32 v1, v9, v11
	v_cvt_pk_fp8_f32 v1, v10, v12 op_sel:[0,0,1]
	global_store_dword v[4:5], v1, off offset:2112
.LBB0_747:
	s_or_b64 exec, exec, s[0:1]
	v_mul_f32_e32 v2, v22, v2
	s_waitcnt lgkmcnt(0)
	s_nop 1
	v_mov_b32_dpp v10, v2 quad_perm:[1,1,1,1] row_mask:0xf bank_mask:0xf
	v_mov_b32_dpp v9, v2 quad_perm:[2,2,2,2] row_mask:0xf bank_mask:0xf
	v_mov_b32_dpp v11, v2 quad_perm:[3,3,3,3] row_mask:0xf bank_mask:0xf
	s_and_saveexec_b64 s[0:1], s[6:7]
	s_cbranch_execz .LBB0_749
	v_mov_b32_e32 v1, v3
	s_waitcnt lgkmcnt(0)
	v_cvt_pk_fp8_f32 v1, v2, v10
	v_cvt_pk_fp8_f32 v1, v9, v11 op_sel:[0,0,1]
	global_store_dword v[4:5], v1, off offset:2144
.LBB0_749:
	s_or_b64 exec, exec, s[0:1]
	v_rcp_f32_e32 v2, v87
	s_waitcnt lgkmcnt(0)
	v_mul_f32_e32 v9, v71, v2
	s_nop 1
	v_mov_b32_dpp v11, v9 quad_perm:[1,1,1,1] row_mask:0xf bank_mask:0xf
	v_mov_b32_dpp v10, v9 quad_perm:[2,2,2,2] row_mask:0xf bank_mask:0xf
	v_mov_b32_dpp v12, v9 quad_perm:[3,3,3,3] row_mask:0xf bank_mask:0xf
	s_and_saveexec_b64 s[0:1], s[6:7]
	s_cbranch_execz .LBB0_751
	v_mov_b32_e32 v1, v3
	s_waitcnt lgkmcnt(0)
	v_cvt_pk_fp8_f32 v1, v9, v11
	v_cvt_pk_fp8_f32 v1, v10, v12 op_sel:[0,0,1]
	global_store_dword v[4:5], v1, off offset:3072
.LBB0_751:
	s_or_b64 exec, exec, s[0:1]
	v_mul_f32_e32 v9, v55, v2
	s_waitcnt lgkmcnt(0)
	s_nop 1
	v_mov_b32_dpp v11, v9 quad_perm:[1,1,1,1] row_mask:0xf bank_mask:0xf
	v_mov_b32_dpp v10, v9 quad_perm:[2,2,2,2] row_mask:0xf bank_mask:0xf
	v_mov_b32_dpp v12, v9 quad_perm:[3,3,3,3] row_mask:0xf bank_mask:0xf
	s_and_saveexec_b64 s[0:1], s[6:7]
	s_cbranch_execz .LBB0_753
	v_mov_b32_e32 v1, v3
	s_waitcnt lgkmcnt(0)
	v_cvt_pk_fp8_f32 v1, v9, v11
	v_cvt_pk_fp8_f32 v1, v10, v12 op_sel:[0,0,1]
	global_store_dword v[4:5], v1, off offset:3104
.LBB0_753:
	s_or_b64 exec, exec, s[0:1]
	v_mul_f32_e32 v9, v39, v2
	s_waitcnt lgkmcnt(0)
	s_nop 1
	v_mov_b32_dpp v11, v9 quad_perm:[1,1,1,1] row_mask:0xf bank_mask:0xf
	v_mov_b32_dpp v10, v9 quad_perm:[2,2,2,2] row_mask:0xf bank_mask:0xf
	v_mov_b32_dpp v12, v9 quad_perm:[3,3,3,3] row_mask:0xf bank_mask:0xf
	s_and_saveexec_b64 s[0:1], s[6:7]
	s_cbranch_execz .LBB0_755
	v_mov_b32_e32 v1, v3
	s_waitcnt lgkmcnt(0)
	v_cvt_pk_fp8_f32 v1, v9, v11
	v_cvt_pk_fp8_f32 v1, v10, v12 op_sel:[0,0,1]
	global_store_dword v[4:5], v1, off offset:3136
.LBB0_755:
	s_or_b64 exec, exec, s[0:1]
	v_mul_f32_e32 v2, v23, v2
	s_waitcnt lgkmcnt(0)
	s_nop 1
	v_mov_b32_dpp v10, v2 quad_perm:[1,1,1,1] row_mask:0xf bank_mask:0xf
	v_mov_b32_dpp v9, v2 quad_perm:[2,2,2,2] row_mask:0xf bank_mask:0xf
	v_mov_b32_dpp v11, v2 quad_perm:[3,3,3,3] row_mask:0xf bank_mask:0xf
	s_and_saveexec_b64 s[0:1], s[6:7]
	s_cbranch_execz .LBB0_757
	v_mov_b32_e32 v1, v3
	s_waitcnt lgkmcnt(0)
	v_cvt_pk_fp8_f32 v1, v2, v10
	v_cvt_pk_fp8_f32 v1, v9, v11 op_sel:[0,0,1]
	global_store_dword v[4:5], v1, off offset:3168
.LBB0_757:
	s_or_b64 exec, exec, s[0:1]
	v_rcp_f32_e32 v2, v88
	s_waitcnt lgkmcnt(0)
	v_mul_f32_e32 v9, v72, v2
	s_nop 1
	v_mov_b32_dpp v11, v9 quad_perm:[1,1,1,1] row_mask:0xf bank_mask:0xf
	v_mov_b32_dpp v10, v9 quad_perm:[2,2,2,2] row_mask:0xf bank_mask:0xf
	v_mov_b32_dpp v12, v9 quad_perm:[3,3,3,3] row_mask:0xf bank_mask:0xf
	s_and_saveexec_b64 s[0:1], s[6:7]
	s_cbranch_execz .LBB0_759
	v_mov_b32_e32 v1, v3
	s_waitcnt lgkmcnt(0)
	v_cvt_pk_fp8_f32 v1, v9, v11
	v_cvt_pk_fp8_f32 v1, v10, v12 op_sel:[0,0,1]
	v_add_co_u32_e32 v10, vcc, 0x2000, v4
	s_nop 1
	v_addc_co_u32_e32 v11, vcc, 0, v5, vcc
	global_store_dword v[10:11], v1, off
.LBB0_759:
	s_or_b64 exec, exec, s[0:1]
	v_mul_f32_e32 v9, v56, v2
	s_waitcnt lgkmcnt(0)
	s_nop 1
	v_mov_b32_dpp v11, v9 quad_perm:[1,1,1,1] row_mask:0xf bank_mask:0xf
	v_mov_b32_dpp v10, v9 quad_perm:[2,2,2,2] row_mask:0xf bank_mask:0xf
	v_mov_b32_dpp v12, v9 quad_perm:[3,3,3,3] row_mask:0xf bank_mask:0xf
	s_and_saveexec_b64 s[0:1], s[6:7]
	s_cbranch_execz .LBB0_761
	v_mov_b32_e32 v1, v3
	s_waitcnt lgkmcnt(0)
	v_cvt_pk_fp8_f32 v1, v9, v11
	v_cvt_pk_fp8_f32 v1, v10, v12 op_sel:[0,0,1]
	v_add_co_u32_e32 v10, vcc, 0x2000, v4
	s_nop 1
	v_addc_co_u32_e32 v11, vcc, 0, v5, vcc
	global_store_dword v[10:11], v1, off offset:32
.LBB0_761:
	s_or_b64 exec, exec, s[0:1]
	v_mul_f32_e32 v9, v40, v2
	s_waitcnt lgkmcnt(0)
	s_nop 1
	v_mov_b32_dpp v11, v9 quad_perm:[1,1,1,1] row_mask:0xf bank_mask:0xf
	v_mov_b32_dpp v10, v9 quad_perm:[2,2,2,2] row_mask:0xf bank_mask:0xf
	v_mov_b32_dpp v12, v9 quad_perm:[3,3,3,3] row_mask:0xf bank_mask:0xf
	s_and_saveexec_b64 s[0:1], s[6:7]
	s_cbranch_execz .LBB0_763
	v_mov_b32_e32 v1, v3
	s_waitcnt lgkmcnt(0)
	v_cvt_pk_fp8_f32 v1, v9, v11
	v_cvt_pk_fp8_f32 v1, v10, v12 op_sel:[0,0,1]
	v_add_co_u32_e32 v10, vcc, 0x2000, v4
	s_nop 1
	v_addc_co_u32_e32 v11, vcc, 0, v5, vcc
	global_store_dword v[10:11], v1, off offset:64
.LBB0_763:
	s_or_b64 exec, exec, s[0:1]
	v_mul_f32_e32 v2, v24, v2
	s_waitcnt lgkmcnt(0)
	s_nop 1
	v_mov_b32_dpp v10, v2 quad_perm:[1,1,1,1] row_mask:0xf bank_mask:0xf
	v_mov_b32_dpp v9, v2 quad_perm:[2,2,2,2] row_mask:0xf bank_mask:0xf
	v_mov_b32_dpp v11, v2 quad_perm:[3,3,3,3] row_mask:0xf bank_mask:0xf
	s_and_saveexec_b64 s[0:1], s[6:7]
	s_cbranch_execz .LBB0_765
	v_mov_b32_e32 v1, v3
	s_waitcnt lgkmcnt(0)
	v_cvt_pk_fp8_f32 v1, v2, v10
	v_add_co_u32_e32 v10, vcc, 0x2000, v4
	v_cvt_pk_fp8_f32 v1, v9, v11 op_sel:[0,0,1]
	s_nop 0
	v_addc_co_u32_e32 v11, vcc, 0, v5, vcc
	global_store_dword v[10:11], v1, off offset:96
.LBB0_765:
	s_or_b64 exec, exec, s[0:1]
	v_rcp_f32_e32 v2, v89
	s_waitcnt lgkmcnt(0)
	v_mul_f32_e32 v9, v73, v2
	s_nop 1
	v_mov_b32_dpp v11, v9 quad_perm:[1,1,1,1] row_mask:0xf bank_mask:0xf
	v_mov_b32_dpp v10, v9 quad_perm:[2,2,2,2] row_mask:0xf bank_mask:0xf
	v_mov_b32_dpp v12, v9 quad_perm:[3,3,3,3] row_mask:0xf bank_mask:0xf
	s_and_saveexec_b64 s[0:1], s[6:7]
	s_cbranch_execz .LBB0_767
	v_mov_b32_e32 v1, v3
	s_waitcnt lgkmcnt(0)
	v_cvt_pk_fp8_f32 v1, v9, v11
	v_cvt_pk_fp8_f32 v1, v10, v12 op_sel:[0,0,1]
	v_add_co_u32_e32 v10, vcc, 0x2000, v4
	s_nop 1
	v_addc_co_u32_e32 v11, vcc, 0, v5, vcc
	global_store_dword v[10:11], v1, off offset:1024
.LBB0_767:
	s_or_b64 exec, exec, s[0:1]
	v_mul_f32_e32 v9, v57, v2
	s_waitcnt lgkmcnt(0)
	s_nop 1
	v_mov_b32_dpp v11, v9 quad_perm:[1,1,1,1] row_mask:0xf bank_mask:0xf
	v_mov_b32_dpp v10, v9 quad_perm:[2,2,2,2] row_mask:0xf bank_mask:0xf
	v_mov_b32_dpp v12, v9 quad_perm:[3,3,3,3] row_mask:0xf bank_mask:0xf
	s_and_saveexec_b64 s[0:1], s[6:7]
	s_cbranch_execz .LBB0_769
	v_mov_b32_e32 v1, v3
	s_waitcnt lgkmcnt(0)
	v_cvt_pk_fp8_f32 v1, v9, v11
	v_cvt_pk_fp8_f32 v1, v10, v12 op_sel:[0,0,1]
	v_add_co_u32_e32 v10, vcc, 0x2000, v4
	s_nop 1
	v_addc_co_u32_e32 v11, vcc, 0, v5, vcc
	global_store_dword v[10:11], v1, off offset:1056
.LBB0_769:
	s_or_b64 exec, exec, s[0:1]
	v_mul_f32_e32 v9, v41, v2
	s_waitcnt lgkmcnt(0)
	s_nop 1
	v_mov_b32_dpp v11, v9 quad_perm:[1,1,1,1] row_mask:0xf bank_mask:0xf
	v_mov_b32_dpp v10, v9 quad_perm:[2,2,2,2] row_mask:0xf bank_mask:0xf
	v_mov_b32_dpp v12, v9 quad_perm:[3,3,3,3] row_mask:0xf bank_mask:0xf
	s_and_saveexec_b64 s[0:1], s[6:7]
	s_cbranch_execz .LBB0_771
	v_mov_b32_e32 v1, v3
	s_waitcnt lgkmcnt(0)
	v_cvt_pk_fp8_f32 v1, v9, v11
	v_cvt_pk_fp8_f32 v1, v10, v12 op_sel:[0,0,1]
	v_add_co_u32_e32 v10, vcc, 0x2000, v4
	s_nop 1
	v_addc_co_u32_e32 v11, vcc, 0, v5, vcc
	global_store_dword v[10:11], v1, off offset:1088
.LBB0_771:
	s_or_b64 exec, exec, s[0:1]
	v_mul_f32_e32 v2, v25, v2
	s_waitcnt lgkmcnt(0)
	s_nop 1
	v_mov_b32_dpp v10, v2 quad_perm:[1,1,1,1] row_mask:0xf bank_mask:0xf
	v_mov_b32_dpp v9, v2 quad_perm:[2,2,2,2] row_mask:0xf bank_mask:0xf
	v_mov_b32_dpp v11, v2 quad_perm:[3,3,3,3] row_mask:0xf bank_mask:0xf
	s_and_saveexec_b64 s[0:1], s[6:7]
	s_cbranch_execz .LBB0_773
	v_mov_b32_e32 v1, v3
	s_waitcnt lgkmcnt(0)
	v_cvt_pk_fp8_f32 v1, v2, v10
	v_add_co_u32_e32 v10, vcc, 0x2000, v4
	v_cvt_pk_fp8_f32 v1, v9, v11 op_sel:[0,0,1]
	s_nop 0
	v_addc_co_u32_e32 v11, vcc, 0, v5, vcc
	global_store_dword v[10:11], v1, off offset:1120
.LBB0_773:
	s_or_b64 exec, exec, s[0:1]
	v_rcp_f32_e32 v2, v90
	s_waitcnt lgkmcnt(0)
	v_mul_f32_e32 v9, v74, v2
	s_nop 1
	v_mov_b32_dpp v11, v9 quad_perm:[1,1,1,1] row_mask:0xf bank_mask:0xf
	v_mov_b32_dpp v10, v9 quad_perm:[2,2,2,2] row_mask:0xf bank_mask:0xf
	v_mov_b32_dpp v12, v9 quad_perm:[3,3,3,3] row_mask:0xf bank_mask:0xf
	s_and_saveexec_b64 s[0:1], s[6:7]
	s_cbranch_execz .LBB0_775
	v_mov_b32_e32 v1, v3
	s_waitcnt lgkmcnt(0)
	v_cvt_pk_fp8_f32 v1, v9, v11
	v_cvt_pk_fp8_f32 v1, v10, v12 op_sel:[0,0,1]
	v_add_co_u32_e32 v10, vcc, 0x2000, v4
	s_nop 1
	v_addc_co_u32_e32 v11, vcc, 0, v5, vcc
	global_store_dword v[10:11], v1, off offset:2048
.LBB0_775:
	s_or_b64 exec, exec, s[0:1]
	v_mul_f32_e32 v9, v58, v2
	s_waitcnt lgkmcnt(0)
	s_nop 1
	v_mov_b32_dpp v11, v9 quad_perm:[1,1,1,1] row_mask:0xf bank_mask:0xf
	v_mov_b32_dpp v10, v9 quad_perm:[2,2,2,2] row_mask:0xf bank_mask:0xf
	v_mov_b32_dpp v12, v9 quad_perm:[3,3,3,3] row_mask:0xf bank_mask:0xf
	s_and_saveexec_b64 s[0:1], s[6:7]
	s_cbranch_execz .LBB0_777
	v_mov_b32_e32 v1, v3
	s_waitcnt lgkmcnt(0)
	v_cvt_pk_fp8_f32 v1, v9, v11
	v_cvt_pk_fp8_f32 v1, v10, v12 op_sel:[0,0,1]
	v_add_co_u32_e32 v10, vcc, 0x2000, v4
	s_nop 1
	v_addc_co_u32_e32 v11, vcc, 0, v5, vcc
	global_store_dword v[10:11], v1, off offset:2080
.LBB0_777:
	s_or_b64 exec, exec, s[0:1]
	v_mul_f32_e32 v9, v42, v2
	s_waitcnt lgkmcnt(0)
	s_nop 1
	v_mov_b32_dpp v11, v9 quad_perm:[1,1,1,1] row_mask:0xf bank_mask:0xf
	v_mov_b32_dpp v10, v9 quad_perm:[2,2,2,2] row_mask:0xf bank_mask:0xf
	v_mov_b32_dpp v12, v9 quad_perm:[3,3,3,3] row_mask:0xf bank_mask:0xf
	s_and_saveexec_b64 s[0:1], s[6:7]
	s_cbranch_execz .LBB0_779
	v_mov_b32_e32 v1, v3
	s_waitcnt lgkmcnt(0)
	v_cvt_pk_fp8_f32 v1, v9, v11
	v_cvt_pk_fp8_f32 v1, v10, v12 op_sel:[0,0,1]
	v_add_co_u32_e32 v10, vcc, 0x2000, v4
	s_nop 1
	v_addc_co_u32_e32 v11, vcc, 0, v5, vcc
	global_store_dword v[10:11], v1, off offset:2112
.LBB0_779:
	s_or_b64 exec, exec, s[0:1]
	v_mul_f32_e32 v2, v26, v2
	s_waitcnt lgkmcnt(0)
	s_nop 1
	v_mov_b32_dpp v10, v2 quad_perm:[1,1,1,1] row_mask:0xf bank_mask:0xf
	v_mov_b32_dpp v9, v2 quad_perm:[2,2,2,2] row_mask:0xf bank_mask:0xf
	v_mov_b32_dpp v11, v2 quad_perm:[3,3,3,3] row_mask:0xf bank_mask:0xf
	s_and_saveexec_b64 s[0:1], s[6:7]
	s_cbranch_execz .LBB0_781
	v_mov_b32_e32 v1, v3
	s_waitcnt lgkmcnt(0)
	v_cvt_pk_fp8_f32 v1, v2, v10
	v_add_co_u32_e32 v10, vcc, 0x2000, v4
	v_cvt_pk_fp8_f32 v1, v9, v11 op_sel:[0,0,1]
	s_nop 0
	v_addc_co_u32_e32 v11, vcc, 0, v5, vcc
	global_store_dword v[10:11], v1, off offset:2144
.LBB0_781:
	s_or_b64 exec, exec, s[0:1]
	v_rcp_f32_e32 v2, v91
	s_waitcnt lgkmcnt(0)
	v_mul_f32_e32 v9, v75, v2
	s_nop 1
	v_mov_b32_dpp v11, v9 quad_perm:[1,1,1,1] row_mask:0xf bank_mask:0xf
	v_mov_b32_dpp v10, v9 quad_perm:[2,2,2,2] row_mask:0xf bank_mask:0xf
	v_mov_b32_dpp v12, v9 quad_perm:[3,3,3,3] row_mask:0xf bank_mask:0xf
	s_and_saveexec_b64 s[0:1], s[6:7]
	s_cbranch_execz .LBB0_783
	v_mov_b32_e32 v1, v3
	s_waitcnt lgkmcnt(0)
	v_cvt_pk_fp8_f32 v1, v9, v11
	v_cvt_pk_fp8_f32 v1, v10, v12 op_sel:[0,0,1]
	v_add_co_u32_e32 v10, vcc, 0x2000, v4
	s_nop 1
	v_addc_co_u32_e32 v11, vcc, 0, v5, vcc
	global_store_dword v[10:11], v1, off offset:3072
.LBB0_783:
	s_or_b64 exec, exec, s[0:1]
	v_mul_f32_e32 v9, v59, v2
	s_waitcnt lgkmcnt(0)
	s_nop 1
	v_mov_b32_dpp v11, v9 quad_perm:[1,1,1,1] row_mask:0xf bank_mask:0xf
	v_mov_b32_dpp v10, v9 quad_perm:[2,2,2,2] row_mask:0xf bank_mask:0xf
	v_mov_b32_dpp v12, v9 quad_perm:[3,3,3,3] row_mask:0xf bank_mask:0xf
	s_and_saveexec_b64 s[0:1], s[6:7]
	s_cbranch_execz .LBB0_785
	v_mov_b32_e32 v1, v3
	s_waitcnt lgkmcnt(0)
	v_cvt_pk_fp8_f32 v1, v9, v11
	v_cvt_pk_fp8_f32 v1, v10, v12 op_sel:[0,0,1]
	v_add_co_u32_e32 v10, vcc, 0x2000, v4
	s_nop 1
	v_addc_co_u32_e32 v11, vcc, 0, v5, vcc
	global_store_dword v[10:11], v1, off offset:3104
.LBB0_785:
	s_or_b64 exec, exec, s[0:1]
	v_mul_f32_e32 v9, v43, v2
	s_waitcnt lgkmcnt(0)
	s_nop 1
	v_mov_b32_dpp v11, v9 quad_perm:[1,1,1,1] row_mask:0xf bank_mask:0xf
	v_mov_b32_dpp v10, v9 quad_perm:[2,2,2,2] row_mask:0xf bank_mask:0xf
	v_mov_b32_dpp v12, v9 quad_perm:[3,3,3,3] row_mask:0xf bank_mask:0xf
	s_and_saveexec_b64 s[0:1], s[6:7]
	s_cbranch_execz .LBB0_787
	v_mov_b32_e32 v1, v3
	s_waitcnt lgkmcnt(0)
	v_cvt_pk_fp8_f32 v1, v9, v11
	v_cvt_pk_fp8_f32 v1, v10, v12 op_sel:[0,0,1]
	v_add_co_u32_e32 v10, vcc, 0x2000, v4
	s_nop 1
	v_addc_co_u32_e32 v11, vcc, 0, v5, vcc
	global_store_dword v[10:11], v1, off offset:3136
.LBB0_787:
	s_or_b64 exec, exec, s[0:1]
	v_mul_f32_e32 v2, v27, v2
	s_waitcnt lgkmcnt(0)
	s_nop 1
	v_mov_b32_dpp v10, v2 quad_perm:[1,1,1,1] row_mask:0xf bank_mask:0xf
	v_mov_b32_dpp v9, v2 quad_perm:[2,2,2,2] row_mask:0xf bank_mask:0xf
	v_mov_b32_dpp v11, v2 quad_perm:[3,3,3,3] row_mask:0xf bank_mask:0xf
	s_and_saveexec_b64 s[0:1], s[6:7]
	s_cbranch_execz .LBB0_789
	v_mov_b32_e32 v1, v3
	s_waitcnt lgkmcnt(0)
	v_cvt_pk_fp8_f32 v1, v2, v10
	v_add_co_u32_e32 v10, vcc, 0x2000, v4
	v_cvt_pk_fp8_f32 v1, v9, v11 op_sel:[0,0,1]
	s_nop 0
	v_addc_co_u32_e32 v11, vcc, 0, v5, vcc
	global_store_dword v[10:11], v1, off offset:3168
.LBB0_789:
	s_or_b64 exec, exec, s[0:1]
	v_rcp_f32_e32 v2, v92
	s_waitcnt lgkmcnt(0)
	v_mul_f32_e32 v9, v76, v2
	s_nop 1
	v_mov_b32_dpp v11, v9 quad_perm:[1,1,1,1] row_mask:0xf bank_mask:0xf
	v_mov_b32_dpp v10, v9 quad_perm:[2,2,2,2] row_mask:0xf bank_mask:0xf
	v_mov_b32_dpp v12, v9 quad_perm:[3,3,3,3] row_mask:0xf bank_mask:0xf
	s_and_saveexec_b64 s[0:1], s[6:7]
	s_cbranch_execz .LBB0_791
	v_mov_b32_e32 v1, v3
	s_waitcnt lgkmcnt(0)
	v_cvt_pk_fp8_f32 v1, v9, v11
	v_cvt_pk_fp8_f32 v1, v10, v12 op_sel:[0,0,1]
	v_add_co_u32_e32 v10, vcc, 0x4000, v4
	s_nop 1
	v_addc_co_u32_e32 v11, vcc, 0, v5, vcc
	global_store_dword v[10:11], v1, off
.LBB0_791:
	s_or_b64 exec, exec, s[0:1]
	v_mul_f32_e32 v9, v60, v2
	s_waitcnt lgkmcnt(0)
	s_nop 1
	v_mov_b32_dpp v11, v9 quad_perm:[1,1,1,1] row_mask:0xf bank_mask:0xf
	v_mov_b32_dpp v10, v9 quad_perm:[2,2,2,2] row_mask:0xf bank_mask:0xf
	v_mov_b32_dpp v12, v9 quad_perm:[3,3,3,3] row_mask:0xf bank_mask:0xf
	s_and_saveexec_b64 s[0:1], s[6:7]
	s_cbranch_execz .LBB0_793
	v_mov_b32_e32 v1, v3
	s_waitcnt lgkmcnt(0)
	v_cvt_pk_fp8_f32 v1, v9, v11
	v_cvt_pk_fp8_f32 v1, v10, v12 op_sel:[0,0,1]
	v_add_co_u32_e32 v10, vcc, 0x4000, v4
	s_nop 1
	v_addc_co_u32_e32 v11, vcc, 0, v5, vcc
	global_store_dword v[10:11], v1, off offset:32
.LBB0_793:
	s_or_b64 exec, exec, s[0:1]
	v_mul_f32_e32 v9, v44, v2
	s_waitcnt lgkmcnt(0)
	s_nop 1
	v_mov_b32_dpp v11, v9 quad_perm:[1,1,1,1] row_mask:0xf bank_mask:0xf
	v_mov_b32_dpp v10, v9 quad_perm:[2,2,2,2] row_mask:0xf bank_mask:0xf
	v_mov_b32_dpp v12, v9 quad_perm:[3,3,3,3] row_mask:0xf bank_mask:0xf
	s_and_saveexec_b64 s[0:1], s[6:7]
	s_cbranch_execz .LBB0_795
	v_mov_b32_e32 v1, v3
	s_waitcnt lgkmcnt(0)
	v_cvt_pk_fp8_f32 v1, v9, v11
	v_cvt_pk_fp8_f32 v1, v10, v12 op_sel:[0,0,1]
	v_add_co_u32_e32 v10, vcc, 0x4000, v4
	s_nop 1
	v_addc_co_u32_e32 v11, vcc, 0, v5, vcc
	global_store_dword v[10:11], v1, off offset:64
.LBB0_795:
	s_or_b64 exec, exec, s[0:1]
	v_mul_f32_e32 v2, v28, v2
	s_waitcnt lgkmcnt(0)
	s_nop 1
	v_mov_b32_dpp v10, v2 quad_perm:[1,1,1,1] row_mask:0xf bank_mask:0xf
	v_mov_b32_dpp v9, v2 quad_perm:[2,2,2,2] row_mask:0xf bank_mask:0xf
	v_mov_b32_dpp v11, v2 quad_perm:[3,3,3,3] row_mask:0xf bank_mask:0xf
	s_and_saveexec_b64 s[0:1], s[6:7]
	s_cbranch_execz .LBB0_797
	v_mov_b32_e32 v1, v3
	s_waitcnt lgkmcnt(0)
	v_cvt_pk_fp8_f32 v1, v2, v10
	v_add_co_u32_e32 v10, vcc, 0x4000, v4
	v_cvt_pk_fp8_f32 v1, v9, v11 op_sel:[0,0,1]
	s_nop 0
	v_addc_co_u32_e32 v11, vcc, 0, v5, vcc
	global_store_dword v[10:11], v1, off offset:96
.LBB0_797:
	s_or_b64 exec, exec, s[0:1]
	v_rcp_f32_e32 v2, v93
	s_waitcnt lgkmcnt(0)
	v_mul_f32_e32 v9, v77, v2
	s_nop 1
	v_mov_b32_dpp v11, v9 quad_perm:[1,1,1,1] row_mask:0xf bank_mask:0xf
	v_mov_b32_dpp v10, v9 quad_perm:[2,2,2,2] row_mask:0xf bank_mask:0xf
	v_mov_b32_dpp v12, v9 quad_perm:[3,3,3,3] row_mask:0xf bank_mask:0xf
	s_and_saveexec_b64 s[0:1], s[6:7]
	s_cbranch_execz .LBB0_799
	v_mov_b32_e32 v1, v3
	s_waitcnt lgkmcnt(0)
	v_cvt_pk_fp8_f32 v1, v9, v11
	v_cvt_pk_fp8_f32 v1, v10, v12 op_sel:[0,0,1]
	v_add_co_u32_e32 v10, vcc, 0x4000, v4
	s_nop 1
	v_addc_co_u32_e32 v11, vcc, 0, v5, vcc
	global_store_dword v[10:11], v1, off offset:1024
.LBB0_799:
	s_or_b64 exec, exec, s[0:1]
	v_mul_f32_e32 v9, v61, v2
	s_waitcnt lgkmcnt(0)
	s_nop 1
	v_mov_b32_dpp v11, v9 quad_perm:[1,1,1,1] row_mask:0xf bank_mask:0xf
	v_mov_b32_dpp v10, v9 quad_perm:[2,2,2,2] row_mask:0xf bank_mask:0xf
	v_mov_b32_dpp v12, v9 quad_perm:[3,3,3,3] row_mask:0xf bank_mask:0xf
	s_and_saveexec_b64 s[0:1], s[6:7]
	s_cbranch_execz .LBB0_801
	v_mov_b32_e32 v1, v3
	s_waitcnt lgkmcnt(0)
	v_cvt_pk_fp8_f32 v1, v9, v11
	v_cvt_pk_fp8_f32 v1, v10, v12 op_sel:[0,0,1]
	v_add_co_u32_e32 v10, vcc, 0x4000, v4
	s_nop 1
	v_addc_co_u32_e32 v11, vcc, 0, v5, vcc
	global_store_dword v[10:11], v1, off offset:1056
.LBB0_801:
	s_or_b64 exec, exec, s[0:1]
	v_mul_f32_e32 v9, v45, v2
	s_waitcnt lgkmcnt(0)
	s_nop 1
	v_mov_b32_dpp v11, v9 quad_perm:[1,1,1,1] row_mask:0xf bank_mask:0xf
	v_mov_b32_dpp v10, v9 quad_perm:[2,2,2,2] row_mask:0xf bank_mask:0xf
	v_mov_b32_dpp v12, v9 quad_perm:[3,3,3,3] row_mask:0xf bank_mask:0xf
	s_and_saveexec_b64 s[0:1], s[6:7]
	s_cbranch_execz .LBB0_803
	v_mov_b32_e32 v1, v3
	s_waitcnt lgkmcnt(0)
	v_cvt_pk_fp8_f32 v1, v9, v11
	v_cvt_pk_fp8_f32 v1, v10, v12 op_sel:[0,0,1]
	v_add_co_u32_e32 v10, vcc, 0x4000, v4
	s_nop 1
	v_addc_co_u32_e32 v11, vcc, 0, v5, vcc
	global_store_dword v[10:11], v1, off offset:1088
.LBB0_803:
	s_or_b64 exec, exec, s[0:1]
	v_mul_f32_e32 v2, v29, v2
	s_waitcnt lgkmcnt(0)
	s_nop 1
	v_mov_b32_dpp v10, v2 quad_perm:[1,1,1,1] row_mask:0xf bank_mask:0xf
	v_mov_b32_dpp v9, v2 quad_perm:[2,2,2,2] row_mask:0xf bank_mask:0xf
	v_mov_b32_dpp v11, v2 quad_perm:[3,3,3,3] row_mask:0xf bank_mask:0xf
	s_and_saveexec_b64 s[0:1], s[6:7]
	s_cbranch_execz .LBB0_805
	v_mov_b32_e32 v1, v3
	s_waitcnt lgkmcnt(0)
	v_cvt_pk_fp8_f32 v1, v2, v10
	v_add_co_u32_e32 v10, vcc, 0x4000, v4
	v_cvt_pk_fp8_f32 v1, v9, v11 op_sel:[0,0,1]
	s_nop 0
	v_addc_co_u32_e32 v11, vcc, 0, v5, vcc
	global_store_dword v[10:11], v1, off offset:1120
.LBB0_805:
	s_or_b64 exec, exec, s[0:1]
	v_rcp_f32_e32 v2, v94
	s_waitcnt lgkmcnt(0)
	v_mul_f32_e32 v9, v78, v2
	s_nop 1
	v_mov_b32_dpp v11, v9 quad_perm:[1,1,1,1] row_mask:0xf bank_mask:0xf
	v_mov_b32_dpp v10, v9 quad_perm:[2,2,2,2] row_mask:0xf bank_mask:0xf
	v_mov_b32_dpp v12, v9 quad_perm:[3,3,3,3] row_mask:0xf bank_mask:0xf
	s_and_saveexec_b64 s[0:1], s[6:7]
	s_cbranch_execz .LBB0_807
	v_mov_b32_e32 v1, v3
	s_waitcnt lgkmcnt(0)
	v_cvt_pk_fp8_f32 v1, v9, v11
	v_cvt_pk_fp8_f32 v1, v10, v12 op_sel:[0,0,1]
	v_add_co_u32_e32 v10, vcc, 0x4000, v4
	s_nop 1
	v_addc_co_u32_e32 v11, vcc, 0, v5, vcc
	global_store_dword v[10:11], v1, off offset:2048
.LBB0_807:
	s_or_b64 exec, exec, s[0:1]
	v_mul_f32_e32 v9, v62, v2
	s_waitcnt lgkmcnt(0)
	s_nop 1
	v_mov_b32_dpp v11, v9 quad_perm:[1,1,1,1] row_mask:0xf bank_mask:0xf
	v_mov_b32_dpp v10, v9 quad_perm:[2,2,2,2] row_mask:0xf bank_mask:0xf
	v_mov_b32_dpp v12, v9 quad_perm:[3,3,3,3] row_mask:0xf bank_mask:0xf
	s_and_saveexec_b64 s[0:1], s[6:7]
	s_cbranch_execz .LBB0_809
	v_mov_b32_e32 v1, v3
	s_waitcnt lgkmcnt(0)
	v_cvt_pk_fp8_f32 v1, v9, v11
	v_cvt_pk_fp8_f32 v1, v10, v12 op_sel:[0,0,1]
	v_add_co_u32_e32 v10, vcc, 0x4000, v4
	s_nop 1
	v_addc_co_u32_e32 v11, vcc, 0, v5, vcc
	global_store_dword v[10:11], v1, off offset:2080
.LBB0_809:
	s_or_b64 exec, exec, s[0:1]
	v_mul_f32_e32 v9, v46, v2
	s_waitcnt lgkmcnt(0)
	s_nop 1
	v_mov_b32_dpp v11, v9 quad_perm:[1,1,1,1] row_mask:0xf bank_mask:0xf
	v_mov_b32_dpp v10, v9 quad_perm:[2,2,2,2] row_mask:0xf bank_mask:0xf
	v_mov_b32_dpp v12, v9 quad_perm:[3,3,3,3] row_mask:0xf bank_mask:0xf
	s_and_saveexec_b64 s[0:1], s[6:7]
	s_cbranch_execz .LBB0_811
	v_mov_b32_e32 v1, v3
	s_waitcnt lgkmcnt(0)
	v_cvt_pk_fp8_f32 v1, v9, v11
	v_cvt_pk_fp8_f32 v1, v10, v12 op_sel:[0,0,1]
	v_add_co_u32_e32 v10, vcc, 0x4000, v4
	s_nop 1
	v_addc_co_u32_e32 v11, vcc, 0, v5, vcc
	global_store_dword v[10:11], v1, off offset:2112
.LBB0_811:
	s_or_b64 exec, exec, s[0:1]
	v_mul_f32_e32 v2, v30, v2
	s_waitcnt lgkmcnt(0)
	s_nop 1
	v_mov_b32_dpp v10, v2 quad_perm:[1,1,1,1] row_mask:0xf bank_mask:0xf
	v_mov_b32_dpp v9, v2 quad_perm:[2,2,2,2] row_mask:0xf bank_mask:0xf
	v_mov_b32_dpp v11, v2 quad_perm:[3,3,3,3] row_mask:0xf bank_mask:0xf
	s_and_saveexec_b64 s[0:1], s[6:7]
	s_cbranch_execz .LBB0_813
	v_mov_b32_e32 v1, v3
	s_waitcnt lgkmcnt(0)
	v_cvt_pk_fp8_f32 v1, v2, v10
	v_add_co_u32_e32 v10, vcc, 0x4000, v4
	v_cvt_pk_fp8_f32 v1, v9, v11 op_sel:[0,0,1]
	s_nop 0
	v_addc_co_u32_e32 v11, vcc, 0, v5, vcc
	global_store_dword v[10:11], v1, off offset:2144
.LBB0_813:
	s_or_b64 exec, exec, s[0:1]
	v_rcp_f32_e32 v2, v95
	s_waitcnt lgkmcnt(0)
	v_mul_f32_e32 v9, v79, v2
	s_nop 1
	v_mov_b32_dpp v11, v9 quad_perm:[1,1,1,1] row_mask:0xf bank_mask:0xf
	v_mov_b32_dpp v10, v9 quad_perm:[2,2,2,2] row_mask:0xf bank_mask:0xf
	v_mov_b32_dpp v12, v9 quad_perm:[3,3,3,3] row_mask:0xf bank_mask:0xf
	s_and_saveexec_b64 s[0:1], s[6:7]
	s_cbranch_execz .LBB0_815
	v_mov_b32_e32 v1, v3
	s_waitcnt lgkmcnt(0)
	v_cvt_pk_fp8_f32 v1, v9, v11
	v_cvt_pk_fp8_f32 v1, v10, v12 op_sel:[0,0,1]
	v_add_co_u32_e32 v10, vcc, 0x4000, v4
	s_nop 1
	v_addc_co_u32_e32 v11, vcc, 0, v5, vcc
	global_store_dword v[10:11], v1, off offset:3072
.LBB0_815:
	s_or_b64 exec, exec, s[0:1]
	v_mul_f32_e32 v9, v63, v2
	s_waitcnt lgkmcnt(0)
	s_nop 1
	v_mov_b32_dpp v11, v9 quad_perm:[1,1,1,1] row_mask:0xf bank_mask:0xf
	v_mov_b32_dpp v10, v9 quad_perm:[2,2,2,2] row_mask:0xf bank_mask:0xf
	v_mov_b32_dpp v12, v9 quad_perm:[3,3,3,3] row_mask:0xf bank_mask:0xf
	s_and_saveexec_b64 s[0:1], s[6:7]
	s_cbranch_execz .LBB0_817
	v_mov_b32_e32 v1, v3
	s_waitcnt lgkmcnt(0)
	v_cvt_pk_fp8_f32 v1, v9, v11
	v_cvt_pk_fp8_f32 v1, v10, v12 op_sel:[0,0,1]
	v_add_co_u32_e32 v10, vcc, 0x4000, v4
	s_nop 1
	v_addc_co_u32_e32 v11, vcc, 0, v5, vcc
	global_store_dword v[10:11], v1, off offset:3104
.LBB0_817:
	s_or_b64 exec, exec, s[0:1]
	v_mul_f32_e32 v9, v47, v2
	s_waitcnt lgkmcnt(0)
	s_nop 1
	v_mov_b32_dpp v11, v9 quad_perm:[1,1,1,1] row_mask:0xf bank_mask:0xf
	v_mov_b32_dpp v10, v9 quad_perm:[2,2,2,2] row_mask:0xf bank_mask:0xf
	v_mov_b32_dpp v12, v9 quad_perm:[3,3,3,3] row_mask:0xf bank_mask:0xf
	s_and_saveexec_b64 s[0:1], s[6:7]
	s_cbranch_execz .LBB0_819
	v_mov_b32_e32 v1, v3
	s_waitcnt lgkmcnt(0)
	v_cvt_pk_fp8_f32 v1, v9, v11
	v_cvt_pk_fp8_f32 v1, v10, v12 op_sel:[0,0,1]
	v_add_co_u32_e32 v10, vcc, 0x4000, v4
	s_nop 1
	v_addc_co_u32_e32 v11, vcc, 0, v5, vcc
	global_store_dword v[10:11], v1, off offset:3136
.LBB0_819:
	s_or_b64 exec, exec, s[0:1]
	v_mul_f32_e32 v2, v31, v2
	s_waitcnt lgkmcnt(0)
	s_nop 1
	v_mov_b32_dpp v10, v2 quad_perm:[1,1,1,1] row_mask:0xf bank_mask:0xf
	v_mov_b32_dpp v9, v2 quad_perm:[2,2,2,2] row_mask:0xf bank_mask:0xf
	v_mov_b32_dpp v11, v2 quad_perm:[3,3,3,3] row_mask:0xf bank_mask:0xf
	s_and_saveexec_b64 s[0:1], s[6:7]
	s_cbranch_execz .LBB0_821
	v_mov_b32_e32 v1, v3
	s_waitcnt lgkmcnt(0)
	v_cvt_pk_fp8_f32 v1, v2, v10
	v_add_co_u32_e32 v10, vcc, 0x4000, v4
	v_cvt_pk_fp8_f32 v1, v9, v11 op_sel:[0,0,1]
	s_nop 0
	v_addc_co_u32_e32 v11, vcc, 0, v5, vcc
	global_store_dword v[10:11], v1, off offset:3168
.LBB0_821:
	s_or_b64 exec, exec, s[0:1]
	v_rcp_f32_e32 v2, v96
	s_waitcnt lgkmcnt(0)
	v_mul_f32_e32 v9, v80, v2
	s_nop 1
	v_mov_b32_dpp v11, v9 quad_perm:[1,1,1,1] row_mask:0xf bank_mask:0xf
	v_mov_b32_dpp v10, v9 quad_perm:[2,2,2,2] row_mask:0xf bank_mask:0xf
	v_mov_b32_dpp v12, v9 quad_perm:[3,3,3,3] row_mask:0xf bank_mask:0xf
	s_and_saveexec_b64 s[0:1], s[6:7]
	s_cbranch_execz .LBB0_823
	v_mov_b32_e32 v1, v3
	s_waitcnt lgkmcnt(0)
	v_cvt_pk_fp8_f32 v1, v9, v11
	v_cvt_pk_fp8_f32 v1, v10, v12 op_sel:[0,0,1]
	v_add_co_u32_e32 v10, vcc, 0x6000, v4
	s_nop 1
	v_addc_co_u32_e32 v11, vcc, 0, v5, vcc
	global_store_dword v[10:11], v1, off
.LBB0_823:
	s_or_b64 exec, exec, s[0:1]
	v_mul_f32_e32 v9, v64, v2
	s_waitcnt lgkmcnt(0)
	s_nop 1
	v_mov_b32_dpp v11, v9 quad_perm:[1,1,1,1] row_mask:0xf bank_mask:0xf
	v_mov_b32_dpp v10, v9 quad_perm:[2,2,2,2] row_mask:0xf bank_mask:0xf
	v_mov_b32_dpp v12, v9 quad_perm:[3,3,3,3] row_mask:0xf bank_mask:0xf
	s_and_saveexec_b64 s[0:1], s[6:7]
	s_cbranch_execz .LBB0_825
	v_mov_b32_e32 v1, v3
	s_waitcnt lgkmcnt(0)
	v_cvt_pk_fp8_f32 v1, v9, v11
	v_cvt_pk_fp8_f32 v1, v10, v12 op_sel:[0,0,1]
	v_add_co_u32_e32 v10, vcc, 0x6000, v4
	s_nop 1
	v_addc_co_u32_e32 v11, vcc, 0, v5, vcc
	global_store_dword v[10:11], v1, off offset:32
.LBB0_825:
	s_or_b64 exec, exec, s[0:1]
	v_mul_f32_e32 v9, v48, v2
	s_waitcnt lgkmcnt(0)
	s_nop 1
	v_mov_b32_dpp v11, v9 quad_perm:[1,1,1,1] row_mask:0xf bank_mask:0xf
	v_mov_b32_dpp v10, v9 quad_perm:[2,2,2,2] row_mask:0xf bank_mask:0xf
	v_mov_b32_dpp v12, v9 quad_perm:[3,3,3,3] row_mask:0xf bank_mask:0xf
	s_and_saveexec_b64 s[0:1], s[6:7]
	s_cbranch_execz .LBB0_827
	v_mov_b32_e32 v1, v3
	s_waitcnt lgkmcnt(0)
	v_cvt_pk_fp8_f32 v1, v9, v11
	v_cvt_pk_fp8_f32 v1, v10, v12 op_sel:[0,0,1]
	v_add_co_u32_e32 v10, vcc, 0x6000, v4
	s_nop 1
	v_addc_co_u32_e32 v11, vcc, 0, v5, vcc
	global_store_dword v[10:11], v1, off offset:64
.LBB0_827:
	s_or_b64 exec, exec, s[0:1]
	v_mul_f32_e32 v2, v32, v2
	s_waitcnt lgkmcnt(0)
	s_nop 1
	v_mov_b32_dpp v10, v2 quad_perm:[1,1,1,1] row_mask:0xf bank_mask:0xf
	v_mov_b32_dpp v9, v2 quad_perm:[2,2,2,2] row_mask:0xf bank_mask:0xf
	v_mov_b32_dpp v11, v2 quad_perm:[3,3,3,3] row_mask:0xf bank_mask:0xf
	s_and_saveexec_b64 s[0:1], s[6:7]
	s_cbranch_execz .LBB0_829
	v_mov_b32_e32 v1, v3
	s_waitcnt lgkmcnt(0)
	v_cvt_pk_fp8_f32 v1, v2, v10
	v_add_co_u32_e32 v10, vcc, 0x6000, v4
	v_cvt_pk_fp8_f32 v1, v9, v11 op_sel:[0,0,1]
	s_nop 0
	v_addc_co_u32_e32 v11, vcc, 0, v5, vcc
	global_store_dword v[10:11], v1, off offset:96
.LBB0_829:
	s_or_b64 exec, exec, s[0:1]
	v_rcp_f32_e32 v2, v97
	s_waitcnt lgkmcnt(0)
	v_mul_f32_e32 v9, v81, v2
	s_nop 1
	v_mov_b32_dpp v11, v9 quad_perm:[1,1,1,1] row_mask:0xf bank_mask:0xf
	v_mov_b32_dpp v10, v9 quad_perm:[2,2,2,2] row_mask:0xf bank_mask:0xf
	v_mov_b32_dpp v12, v9 quad_perm:[3,3,3,3] row_mask:0xf bank_mask:0xf
	s_and_saveexec_b64 s[0:1], s[6:7]
	s_cbranch_execz .LBB0_831
	v_mov_b32_e32 v1, v3
	s_waitcnt lgkmcnt(0)
	v_cvt_pk_fp8_f32 v1, v9, v11
	v_cvt_pk_fp8_f32 v1, v10, v12 op_sel:[0,0,1]
	v_add_co_u32_e32 v10, vcc, 0x6000, v4
	s_nop 1
	v_addc_co_u32_e32 v11, vcc, 0, v5, vcc
	global_store_dword v[10:11], v1, off offset:1024
.LBB0_831:
	s_or_b64 exec, exec, s[0:1]
	v_mul_f32_e32 v9, v65, v2
	s_waitcnt lgkmcnt(0)
	s_nop 1
	v_mov_b32_dpp v11, v9 quad_perm:[1,1,1,1] row_mask:0xf bank_mask:0xf
	v_mov_b32_dpp v10, v9 quad_perm:[2,2,2,2] row_mask:0xf bank_mask:0xf
	v_mov_b32_dpp v12, v9 quad_perm:[3,3,3,3] row_mask:0xf bank_mask:0xf
	s_and_saveexec_b64 s[0:1], s[6:7]
	s_cbranch_execz .LBB0_833
	v_mov_b32_e32 v1, v3
	s_waitcnt lgkmcnt(0)
	v_cvt_pk_fp8_f32 v1, v9, v11
	v_cvt_pk_fp8_f32 v1, v10, v12 op_sel:[0,0,1]
	v_add_co_u32_e32 v10, vcc, 0x6000, v4
	s_nop 1
	v_addc_co_u32_e32 v11, vcc, 0, v5, vcc
	global_store_dword v[10:11], v1, off offset:1056
.LBB0_833:
	s_or_b64 exec, exec, s[0:1]
	v_mul_f32_e32 v9, v49, v2
	s_waitcnt lgkmcnt(0)
	s_nop 1
	v_mov_b32_dpp v11, v9 quad_perm:[1,1,1,1] row_mask:0xf bank_mask:0xf
	v_mov_b32_dpp v10, v9 quad_perm:[2,2,2,2] row_mask:0xf bank_mask:0xf
	v_mov_b32_dpp v12, v9 quad_perm:[3,3,3,3] row_mask:0xf bank_mask:0xf
	s_and_saveexec_b64 s[0:1], s[6:7]
	s_cbranch_execz .LBB0_835
	v_mov_b32_e32 v1, v3
	s_waitcnt lgkmcnt(0)
	v_cvt_pk_fp8_f32 v1, v9, v11
	v_cvt_pk_fp8_f32 v1, v10, v12 op_sel:[0,0,1]
	v_add_co_u32_e32 v10, vcc, 0x6000, v4
	s_nop 1
	v_addc_co_u32_e32 v11, vcc, 0, v5, vcc
	global_store_dword v[10:11], v1, off offset:1088
.LBB0_835:
	s_or_b64 exec, exec, s[0:1]
	v_mul_f32_e32 v2, v33, v2
	s_waitcnt lgkmcnt(0)
	s_nop 1
	v_mov_b32_dpp v10, v2 quad_perm:[1,1,1,1] row_mask:0xf bank_mask:0xf
	v_mov_b32_dpp v9, v2 quad_perm:[2,2,2,2] row_mask:0xf bank_mask:0xf
	v_mov_b32_dpp v11, v2 quad_perm:[3,3,3,3] row_mask:0xf bank_mask:0xf
	s_and_saveexec_b64 s[0:1], s[6:7]
	s_cbranch_execz .LBB0_837
	v_mov_b32_e32 v1, v3
	s_waitcnt lgkmcnt(0)
	v_cvt_pk_fp8_f32 v1, v2, v10
	v_add_co_u32_e32 v10, vcc, 0x6000, v4
	v_cvt_pk_fp8_f32 v1, v9, v11 op_sel:[0,0,1]
	s_nop 0
	v_addc_co_u32_e32 v11, vcc, 0, v5, vcc
	global_store_dword v[10:11], v1, off offset:1120
.LBB0_837:
	s_or_b64 exec, exec, s[0:1]
	v_rcp_f32_e32 v2, v98
	s_waitcnt lgkmcnt(0)
	v_mul_f32_e32 v9, v82, v2
	s_nop 1
	v_mov_b32_dpp v11, v9 quad_perm:[1,1,1,1] row_mask:0xf bank_mask:0xf
	v_mov_b32_dpp v10, v9 quad_perm:[2,2,2,2] row_mask:0xf bank_mask:0xf
	v_mov_b32_dpp v12, v9 quad_perm:[3,3,3,3] row_mask:0xf bank_mask:0xf
	s_and_saveexec_b64 s[0:1], s[6:7]
	s_cbranch_execz .LBB0_839
	v_mov_b32_e32 v1, v3
	s_waitcnt lgkmcnt(0)
	v_cvt_pk_fp8_f32 v1, v9, v11
	v_cvt_pk_fp8_f32 v1, v10, v12 op_sel:[0,0,1]
	v_add_co_u32_e32 v10, vcc, 0x6000, v4
	s_nop 1
	v_addc_co_u32_e32 v11, vcc, 0, v5, vcc
	global_store_dword v[10:11], v1, off offset:2048
.LBB0_839:
	s_or_b64 exec, exec, s[0:1]
	v_mul_f32_e32 v9, v66, v2
	s_waitcnt lgkmcnt(0)
	s_nop 1
	v_mov_b32_dpp v11, v9 quad_perm:[1,1,1,1] row_mask:0xf bank_mask:0xf
	v_mov_b32_dpp v10, v9 quad_perm:[2,2,2,2] row_mask:0xf bank_mask:0xf
	v_mov_b32_dpp v12, v9 quad_perm:[3,3,3,3] row_mask:0xf bank_mask:0xf
	s_and_saveexec_b64 s[0:1], s[6:7]
	s_cbranch_execz .LBB0_841
	v_mov_b32_e32 v1, v3
	s_waitcnt lgkmcnt(0)
	v_cvt_pk_fp8_f32 v1, v9, v11
	v_cvt_pk_fp8_f32 v1, v10, v12 op_sel:[0,0,1]
	v_add_co_u32_e32 v10, vcc, 0x6000, v4
	s_nop 1
	v_addc_co_u32_e32 v11, vcc, 0, v5, vcc
	global_store_dword v[10:11], v1, off offset:2080
.LBB0_841:
	s_or_b64 exec, exec, s[0:1]
	v_mul_f32_e32 v9, v50, v2
	s_waitcnt lgkmcnt(0)
	s_nop 1
	v_mov_b32_dpp v11, v9 quad_perm:[1,1,1,1] row_mask:0xf bank_mask:0xf
	v_mov_b32_dpp v10, v9 quad_perm:[2,2,2,2] row_mask:0xf bank_mask:0xf
	v_mov_b32_dpp v12, v9 quad_perm:[3,3,3,3] row_mask:0xf bank_mask:0xf
	s_and_saveexec_b64 s[0:1], s[6:7]
	s_cbranch_execz .LBB0_843
	v_mov_b32_e32 v1, v3
	s_waitcnt lgkmcnt(0)
	v_cvt_pk_fp8_f32 v1, v9, v11
	v_cvt_pk_fp8_f32 v1, v10, v12 op_sel:[0,0,1]
	v_add_co_u32_e32 v10, vcc, 0x6000, v4
	s_nop 1
	v_addc_co_u32_e32 v11, vcc, 0, v5, vcc
	global_store_dword v[10:11], v1, off offset:2112
.LBB0_843:
	s_or_b64 exec, exec, s[0:1]
	v_mul_f32_e32 v2, v34, v2
	s_waitcnt lgkmcnt(0)
	s_nop 1
	v_mov_b32_dpp v10, v2 quad_perm:[1,1,1,1] row_mask:0xf bank_mask:0xf
	v_mov_b32_dpp v9, v2 quad_perm:[2,2,2,2] row_mask:0xf bank_mask:0xf
	v_mov_b32_dpp v11, v2 quad_perm:[3,3,3,3] row_mask:0xf bank_mask:0xf
	s_and_saveexec_b64 s[0:1], s[6:7]
	s_cbranch_execz .LBB0_845
	v_mov_b32_e32 v1, v3
	s_waitcnt lgkmcnt(0)
	v_cvt_pk_fp8_f32 v1, v2, v10
	v_add_co_u32_e32 v10, vcc, 0x6000, v4
	v_cvt_pk_fp8_f32 v1, v9, v11 op_sel:[0,0,1]
	s_nop 0
	v_addc_co_u32_e32 v11, vcc, 0, v5, vcc
	global_store_dword v[10:11], v1, off offset:2144
.LBB0_845:
	s_or_b64 exec, exec, s[0:1]
	v_rcp_f32_e32 v2, v99
	s_waitcnt lgkmcnt(0)
	v_mul_f32_e32 v9, v83, v2
	s_nop 1
	v_mov_b32_dpp v11, v9 quad_perm:[1,1,1,1] row_mask:0xf bank_mask:0xf
	v_mov_b32_dpp v10, v9 quad_perm:[2,2,2,2] row_mask:0xf bank_mask:0xf
	v_mov_b32_dpp v12, v9 quad_perm:[3,3,3,3] row_mask:0xf bank_mask:0xf
	s_and_saveexec_b64 s[0:1], s[6:7]
	s_cbranch_execz .LBB0_847
	v_mov_b32_e32 v1, v3
	s_waitcnt lgkmcnt(0)
	v_cvt_pk_fp8_f32 v1, v9, v11
	v_cvt_pk_fp8_f32 v1, v10, v12 op_sel:[0,0,1]
	v_add_co_u32_e32 v10, vcc, 0x6000, v4
	s_nop 1
	v_addc_co_u32_e32 v11, vcc, 0, v5, vcc
	global_store_dword v[10:11], v1, off offset:3072
.LBB0_847:
	s_or_b64 exec, exec, s[0:1]
	v_mul_f32_e32 v9, v67, v2
	s_waitcnt lgkmcnt(0)
	s_nop 1
	v_mov_b32_dpp v11, v9 quad_perm:[1,1,1,1] row_mask:0xf bank_mask:0xf
	v_mov_b32_dpp v10, v9 quad_perm:[2,2,2,2] row_mask:0xf bank_mask:0xf
	v_mov_b32_dpp v12, v9 quad_perm:[3,3,3,3] row_mask:0xf bank_mask:0xf
	s_and_saveexec_b64 s[0:1], s[6:7]
	s_cbranch_execz .LBB0_849
	v_mov_b32_e32 v1, v3
	s_waitcnt lgkmcnt(0)
	v_cvt_pk_fp8_f32 v1, v9, v11
	v_cvt_pk_fp8_f32 v1, v10, v12 op_sel:[0,0,1]
	v_add_co_u32_e32 v10, vcc, 0x6000, v4
	s_nop 1
	v_addc_co_u32_e32 v11, vcc, 0, v5, vcc
	global_store_dword v[10:11], v1, off offset:3104
.LBB0_849:
	s_or_b64 exec, exec, s[0:1]
	v_mul_f32_e32 v9, v51, v2
	s_waitcnt lgkmcnt(0)
	s_nop 1
	v_mov_b32_dpp v11, v9 quad_perm:[1,1,1,1] row_mask:0xf bank_mask:0xf
	v_mov_b32_dpp v10, v9 quad_perm:[2,2,2,2] row_mask:0xf bank_mask:0xf
	v_mov_b32_dpp v12, v9 quad_perm:[3,3,3,3] row_mask:0xf bank_mask:0xf
	s_and_saveexec_b64 s[0:1], s[6:7]
	s_cbranch_execz .LBB0_851
	v_mov_b32_e32 v1, v3
	s_waitcnt lgkmcnt(0)
	v_cvt_pk_fp8_f32 v1, v9, v11
	v_cvt_pk_fp8_f32 v1, v10, v12 op_sel:[0,0,1]
	v_add_co_u32_e32 v10, vcc, 0x6000, v4
	s_nop 1
	v_addc_co_u32_e32 v11, vcc, 0, v5, vcc
	global_store_dword v[10:11], v1, off offset:3136
.LBB0_851:
	s_or_b64 exec, exec, s[0:1]
	v_mul_f32_e32 v2, v35, v2
	s_nop 1
	v_mov_b32_dpp v9, v2 quad_perm:[1,1,1,1] row_mask:0xf bank_mask:0xf
	v_mov_b32_dpp v6, v2 quad_perm:[2,2,2,2] row_mask:0xf bank_mask:0xf
	v_mov_b32_dpp v7, v2 quad_perm:[3,3,3,3] row_mask:0xf bank_mask:0xf
	s_and_saveexec_b64 s[0:1], s[6:7]
	s_cbranch_execz .LBB0_691
	v_mov_b32_e32 v1, v3
	s_waitcnt lgkmcnt(0)
	v_cvt_pk_fp8_f32 v1, v2, v9
	v_add_co_u32_e32 v4, vcc, 0x6000, v4
	v_cvt_pk_fp8_f32 v1, v6, v7 op_sel:[0,0,1]
	s_nop 0
	v_addc_co_u32_e32 v5, vcc, 0, v5, vcc
	global_store_dword v[4:5], v1, off offset:3168
	s_branch .LBB0_691
